# plus MoE-up: next unit token-list segment staged into per-wave LDS scratch by one LDS-DMA at unit top; last trip reads row tokens from LDS (no VMEM drain per unit)
# speedup vs baseline: 1.0067x; 1.0067x over previous
; __device__ __forceinline__ int otid() { int t = threadIdx.x; asm volatile("" : "+v"(t)); return t; }
;     __device__ __forceinline__ bool next(int i, pg::Unit& u) const { u.aux = 0; u.aux2 = 0; u.half = 0; return ord.get(i, u.pm, u.pn); }
;     __device__ __forceinline__ bool next(int i, pg::Unit& u) const { u.aux = 0; u.aux2 = 0; u.half = 0; return ord.get(i, u.pm, u.pn); }
; template <class P, class MK = NoChain>
; __device__ __forceinline__ void gemm_phase(LAS unsigned char* lds, const P& p, const MK& mk = MK(), bool chain_out = false, bool chained_in = false) {
;     ...
;     for (;;) {
;         const bool has_next = p.next(ui + 1, nxt);
;         const char* nA = has_next ? p.a_base(nxt) : cA; const char* nB = has_next ? p.b_base(nxt) : cB;
;         const bool chain_now = CHAIN && chain_out && !has_next;
;         if constexpr (CHAIN) { if (chain_now) { const auto np = mk(); Unit nu; (void)np.next(0, nu); nA = np.a_base(nu); nB = np.b_base(nu); } }
;         const bool full = P::HALF ? (cur.half == 0) : true;
;     __device__ __forceinline__ void a_offsets(const pg::Unit& u, unsigned (&off)[2][2]) const {
;         int R[2], C[2]; { const int t_ = otid(); pg::stage_rc(t_ * 16, R[0], C[0]); pg::stage_rc(t_ * 16 + 8192, R[1], C[1]); }
;         if (u.aux < 64) {
;             const int n = T.cnt[u.aux]; const int* lp = LIST + (size_t)u.aux * NT + u.pm * 256;
; #pragma unroll
;             for (int h = 0; h < 2; ++h)
; #pragma unroll
;                 for (int i = 0; i < 2; ++i) { const int r = R[i] + 128 * h; const int tok = (u.pm * 256 + r < n) ? lp[r] : 0; off[h][i] = (unsigned)(tok * K + C[i] * 2); }
.LBB0_1490:
	s_cmp_gt_i32 s24, 63
	s_cselect_b64 s[0:1], -1, 0
	s_ashr_i32 s25, s24, 31
	s_lshl_b64 s[36:37], s[24:25], 15
	s_lshl_b32 s25, s24, 2
	s_add_i32 s25, s25, 0
	s_add_i32 s25, s25, 0x20100
	v_lshlrev_b32_e32 v194, 8, v237
	s_add_u32 s36, s49, s36
	v_ashrrev_i32_e32 v195, 31, v194
	s_addc_u32 s37, s50, s37
	v_lshlrev_b32_e32 v200, 19, v237
	s_waitcnt lgkmcnt(0)
	v_lshlrev_b64 v[2:3], 2, v[194:195]
	s_add_u32 s33, s34, 0x200
	v_or_b32_e32 v201, 0x40000, v200
	v_lshl_add_u64 v[196:197], s[36:37], 0, v[2:3]
	s_addc_u32 s70, s35, 0
	s_mov_b32 s71, 0
	s_mov_b64 s[34:35], s[20:21]
	v_and_b32_e32 v2, 63, v0
	v_lshlrev_b32_e32 v2, 4, v2
	v_mov_b32_e32 v3, 0
	v_lshl_add_u64 v[2:3], v[196:197], 0, v[2:3]
	v_readfirstlane_b32 s36, v0
	s_lshr_b32 s36, s36, 6
	s_lshl_b32 s36, s36, 10
	s_add_i32 s36, s36, 0x21000
	s_mov_b32 m0, s36
	s_nop 0
	global_load_lds_dwordx4 v[2:3], off
	s_barrier
	s_branch .LBB0_1492

; __device__ __forceinline__ int otid() { int t = threadIdx.x; asm volatile("" : "+v"(t)); return t; }
;     __device__ __forceinline__ void a_offsets(const pg::Unit& u, unsigned (&off)[2][2]) const {
;         int R[2], C[2]; { const int t_ = otid(); pg::stage_rc(t_ * 16, R[0], C[0]); pg::stage_rc(t_ * 16 + 8192, R[1], C[1]); }
;         if (u.aux < 64) {
;             const int n = T.cnt[u.aux]; const int* lp = LIST + (size_t)u.aux * NT + u.pm * 256;
; #pragma unroll
;             for (int h = 0; h < 2; ++h)
; #pragma unroll
;                 for (int i = 0; i < 2; ++i) { const int r = R[i] + 128 * h; const int tok = (u.pm * 256 + r < n) ? lp[r] : 0; off[h][i] = (unsigned)(tok * K + C[i] * 2); }
;         } else {
; #pragma unroll
;             for (int h = 0; h < 2; ++h)
; #pragma unroll
;                 for (int i = 0; i < 2; ++i) off[h][i] = (unsigned)((u.pm * 256 + R[i] + 128 * h) * K + C[i] * 2);
;         }
.LBB0_1495:
	s_andn2_b64 vcc, exec, s[40:41]
	s_cbranch_vccnz .LBB0_1505
	v_mov_b32_e32 v13, s25
	ds_read_b32 v9, v13
	v_add_u32_e32 v10, v4, v194
	v_add_u32_e32 v11, v2, v194
	v_readfirstlane_b32 s40, v0
	s_lshr_b32 s40, s40, 6
	s_lshl_b32 s40, s40, 10
	s_add_i32 s40, s40, 0x21000
	v_lshl_add_u32 v5, v4, 2, s40
	v_lshl_add_u32 v3, v2, 2, s40
	ds_read_b32 v8, v5
	ds_read_b32 v7, v3
	ds_read_b32 v12, v5 offset:512
	ds_read_b32 v13, v3 offset:512
	s_waitcnt lgkmcnt(0)
	v_cmp_lt_i32_e64 s[40:41], v10, v9
	v_add_u32_e32 v10, 0x80, v10
	v_cndmask_b32_e64 v8, 0, v8, s[40:41]
	v_cmp_lt_i32_e32 vcc, v11, v9
	v_add_u32_e32 v11, 0x80, v11
	s_nop 0
	v_cndmask_b32_e32 v7, 0, v7, vcc
	v_cmp_lt_i32_e64 s[40:41], v10, v9
	v_lshlrev_b32_e32 v8, 11, v8
	v_lshlrev_b32_e32 v7, 11, v7
	v_cndmask_b32_e64 v12, 0, v12, s[40:41]
	v_cmp_lt_i32_e32 vcc, v11, v9
	v_lshlrev_b32_e32 v12, 11, v12
	s_nop 0
	v_cndmask_b32_e32 v10, 0, v13, vcc
	v_lshlrev_b32_e32 v10, 11, v10
	v_or_b32_e32 v241, v12, v6
	v_or_b32_e32 v210, v7, v6
	v_or_b32_e32 v240, v8, v6
	v_or_b32_e32 v218, v10, v6
